# grid barrier: all waiters poll the TOP arrival counter against (gen+1)*nx, removing the TOPGEN release hop (on top of v22)
# baseline (speedup 1.0000x reference)
.LBB0_476:
	v_readlane_b32 s6, v252, 15
	v_readlane_b32 s7, v252, 16
	v_cvt_f32_u32_e32 v0, v3
	v_sub_u32_e32 v5, 0, v3
	v_rcp_iflag_f32_e32 v0, v0
	s_nop 1
	global_atomic_add v4, v1, v236, s[6:7] sc0
	v_mul_f32_e32 v0, 0x4f7ffffe, v0
	v_cvt_u32_f32_e32 v0, v0
	v_mul_lo_u32 v5, v5, v0
	v_mul_hi_u32 v5, v0, v5
	v_add_u32_e32 v0, v0, v5
	s_waitcnt vmcnt(0)
	v_mul_hi_u32 v0, v4, v0
	v_mul_lo_u32 v5, v0, v3
	v_sub_u32_e32 v5, v4, v5
	v_add_u32_e32 v6, 1, v0
	v_cmp_ge_u32_e32 vcc, v5, v3
	v_add_u32_e32 v4, 1, v4
	s_nop 0
	v_cndmask_b32_e32 v0, v0, v6, vcc
	v_sub_u32_e32 v6, v5, v3
	v_cndmask_b32_e32 v5, v5, v6, vcc
	v_add_u32_e32 v6, 1, v0
	v_cmp_ge_u32_e32 vcc, v5, v3
	s_nop 1
	v_cndmask_b32_e32 v0, v0, v6, vcc
	v_mul_lo_u32 v5, v3, v0
	v_add_u32_e32 v3, v5, v3
	v_cmp_ne_u32_e32 vcc, v4, v3
	s_and_saveexec_b64 s[6:7], vcc
	s_xor_b64 s[6:7], exec, s[6:7]
	s_cbranch_execz .LBB0_490
	v_readlane_b32 s8, v252, 19
	v_readlane_b32 s9, v252, 20
	s_waitcnt lgkmcnt(0)
	v_add_u32_e32 v5, 1, v0
	v_mul_lo_u32 v5, v5, v2
	s_nop 3
	global_load_dword v2, v1, s[8:9] sc1
	s_waitcnt vmcnt(0)
	v_cmp_lt_u32_e32 vcc, v2, v5
	s_and_saveexec_b64 s[8:9], vcc
	s_cbranch_execz .LBB0_489
	s_mov_b32 s13, 1
	s_mov_b64 s[10:11], 0
	s_branch .LBB0_480

.LBB0_482:
	v_readlane_b32 s26, v252, 19
	v_readlane_b32 s27, v252, 20
	s_add_i32 s13, s13, 1
	s_mov_b64 s[34:35], -1
	s_nop 2
	global_load_dword v2, v1, s[26:27] sc1
	s_waitcnt vmcnt(0)
	v_cmp_ge_u32_e32 vcc, v2, v5
	s_orn2_b64 s[30:31], vcc, exec
	s_branch .LBB0_479

.LBB0_493:
	s_or_b64 exec, exec, s[8:9]
	s_waitcnt vmcnt(0)
	v_readfirstlane_b32 s6, v3
	v_sub_u32_e32 v4, 0, v2
	s_mov_b64 s[8:9], -1
	v_add_u32_e32 v3, s6, v0
	v_cvt_f32_u32_e32 v0, v2
	v_readlane_b32 s6, v252, 21
	v_readlane_b32 s7, v252, 22
	v_rcp_iflag_f32_e32 v0, v0
	s_nop 0
	v_mul_f32_e32 v0, 0x4f7ffffe, v0
	v_cvt_u32_f32_e32 v0, v0
	v_mul_lo_u32 v4, v4, v0
	v_mul_hi_u32 v4, v0, v4
	v_add_u32_e32 v0, v0, v4
	v_mul_hi_u32 v0, v3, v0
	v_mul_lo_u32 v4, v0, v2
	v_sub_u32_e32 v4, v3, v4
	v_cmp_ge_u32_e32 vcc, v4, v2
	v_add_u32_e32 v5, 1, v0
	v_add_u32_e32 v3, 1, v3
	v_cndmask_b32_e32 v0, v0, v5, vcc
	v_sub_u32_e32 v5, v4, v2
	v_cndmask_b32_e32 v4, v4, v5, vcc
	v_cmp_ge_u32_e32 vcc, v4, v2
	v_add_u32_e32 v4, 1, v0
	s_nop 0
	v_cndmask_b32_e32 v0, v0, v4, vcc
	v_mul_lo_u32 v4, v2, v0
	v_add_u32_e32 v2, v4, v2
	v_mov_b32_e32 v5, v2
	v_cmp_ne_u32_e32 vcc, v3, v2
	v_mov_b64_e32 v[2:3], s[6:7]
	s_and_saveexec_b64 s[6:7], vcc
	s_cbranch_execz .LBB0_505
	v_readlane_b32 s8, v252, 19
	v_readlane_b32 s9, v252, 20
	s_mov_b64 s[10:11], 0
	s_nop 3
	global_load_dword v2, v1, s[8:9] sc1
	s_waitcnt vmcnt(0)
	v_cmp_lt_u32_e32 vcc, v2, v5
	s_and_saveexec_b64 s[8:9], vcc
	s_cbranch_execz .LBB0_504
	s_mov_b32 s13, 1
	s_branch .LBB0_497

.LBB0_1037:
	v_readlane_b32 s4, v252, 15
	v_readlane_b32 s5, v252, 16
	v_cvt_f32_u32_e32 v0, v3
	v_sub_u32_e32 v5, 0, v3
	v_rcp_iflag_f32_e32 v0, v0
	s_nop 1
	global_atomic_add v4, v1, v236, s[4:5] sc0
	v_mul_f32_e32 v0, 0x4f7ffffe, v0
	v_cvt_u32_f32_e32 v0, v0
	v_mul_lo_u32 v5, v5, v0
	v_mul_hi_u32 v5, v0, v5
	v_add_u32_e32 v0, v0, v5
	s_waitcnt vmcnt(0)
	v_mul_hi_u32 v0, v4, v0
	v_mul_lo_u32 v5, v0, v3
	v_sub_u32_e32 v5, v4, v5
	v_add_u32_e32 v6, 1, v0
	v_cmp_ge_u32_e32 vcc, v5, v3
	v_add_u32_e32 v4, 1, v4
	s_nop 0
	v_cndmask_b32_e32 v0, v0, v6, vcc
	v_sub_u32_e32 v6, v5, v3
	v_cndmask_b32_e32 v5, v5, v6, vcc
	v_add_u32_e32 v6, 1, v0
	v_cmp_ge_u32_e32 vcc, v5, v3
	s_nop 1
	v_cndmask_b32_e32 v0, v0, v6, vcc
	v_mul_lo_u32 v5, v3, v0
	v_add_u32_e32 v3, v5, v3
	v_cmp_ne_u32_e32 vcc, v4, v3
	s_and_saveexec_b64 s[4:5], vcc
	s_xor_b64 s[4:5], exec, s[4:5]
	s_cbranch_execz .LBB0_1051
	v_readlane_b32 s6, v252, 19
	v_readlane_b32 s7, v252, 20
	s_waitcnt lgkmcnt(0)
	v_add_u32_e32 v5, 1, v0
	v_mul_lo_u32 v5, v5, v2
	s_nop 3
	global_load_dword v2, v1, s[6:7] sc1
	s_waitcnt vmcnt(0)
	v_cmp_lt_u32_e32 vcc, v2, v5
	s_and_saveexec_b64 s[6:7], vcc
	s_cbranch_execz .LBB0_1050
	s_mov_b32 s13, 1
	s_mov_b64 s[8:9], 0
	s_branch .LBB0_1041

.LBB0_1043:
	v_readlane_b32 s26, v252, 19
	v_readlane_b32 s27, v252, 20
	s_add_i32 s13, s13, 1
	s_mov_b64 s[30:31], -1
	s_nop 2
	global_load_dword v2, v1, s[26:27] sc1
	s_waitcnt vmcnt(0)
	v_cmp_ge_u32_e32 vcc, v2, v5
	s_orn2_b64 s[28:29], vcc, exec
	s_branch .LBB0_1040

.LBB0_1054:
	s_or_b64 exec, exec, s[6:7]
	s_waitcnt vmcnt(0)
	v_readfirstlane_b32 s4, v3
	v_sub_u32_e32 v4, 0, v2
	s_mov_b64 s[6:7], -1
	v_add_u32_e32 v3, s4, v0
	v_cvt_f32_u32_e32 v0, v2
	v_readlane_b32 s4, v252, 21
	v_readlane_b32 s5, v252, 22
	v_rcp_iflag_f32_e32 v0, v0
	s_nop 0
	v_mul_f32_e32 v0, 0x4f7ffffe, v0
	v_cvt_u32_f32_e32 v0, v0
	v_mul_lo_u32 v4, v4, v0
	v_mul_hi_u32 v4, v0, v4
	v_add_u32_e32 v0, v0, v4
	v_mul_hi_u32 v0, v3, v0
	v_mul_lo_u32 v4, v0, v2
	v_sub_u32_e32 v4, v3, v4
	v_cmp_ge_u32_e32 vcc, v4, v2
	v_add_u32_e32 v5, 1, v0
	v_add_u32_e32 v3, 1, v3
	v_cndmask_b32_e32 v0, v0, v5, vcc
	v_sub_u32_e32 v5, v4, v2
	v_cndmask_b32_e32 v4, v4, v5, vcc
	v_cmp_ge_u32_e32 vcc, v4, v2
	v_add_u32_e32 v4, 1, v0
	s_nop 0
	v_cndmask_b32_e32 v0, v0, v4, vcc
	v_mul_lo_u32 v4, v2, v0
	v_add_u32_e32 v2, v4, v2
	v_mov_b32_e32 v5, v2
	v_cmp_ne_u32_e32 vcc, v3, v2
	v_mov_b64_e32 v[2:3], s[4:5]
	s_and_saveexec_b64 s[4:5], vcc
	s_cbranch_execz .LBB0_1066
	v_readlane_b32 s6, v252, 19
	v_readlane_b32 s7, v252, 20
	s_mov_b64 s[8:9], 0
	s_nop 3
	global_load_dword v2, v1, s[6:7] sc1
	s_waitcnt vmcnt(0)
	v_cmp_lt_u32_e32 vcc, v2, v5
	s_and_saveexec_b64 s[6:7], vcc
	s_cbranch_execz .LBB0_1065
	s_mov_b32 s13, 1
	s_branch .LBB0_1058

.LBB0_1498:
	v_readlane_b32 s0, v252, 15
	v_readlane_b32 s1, v252, 16
	v_cvt_f32_u32_e32 v0, v3
	v_sub_u32_e32 v5, 0, v3
	v_rcp_iflag_f32_e32 v0, v0
	s_nop 1
	global_atomic_add v4, v1, v236, s[0:1] sc0
	v_mul_f32_e32 v0, 0x4f7ffffe, v0
	v_cvt_u32_f32_e32 v0, v0
	v_mul_lo_u32 v5, v5, v0
	v_mul_hi_u32 v5, v0, v5
	v_add_u32_e32 v0, v0, v5
	s_waitcnt vmcnt(0)
	v_mul_hi_u32 v0, v4, v0
	v_mul_lo_u32 v5, v0, v3
	v_sub_u32_e32 v5, v4, v5
	v_add_u32_e32 v6, 1, v0
	v_cmp_ge_u32_e32 vcc, v5, v3
	v_add_u32_e32 v4, 1, v4
	s_nop 0
	v_cndmask_b32_e32 v0, v0, v6, vcc
	v_sub_u32_e32 v6, v5, v3
	v_cndmask_b32_e32 v5, v5, v6, vcc
	v_add_u32_e32 v6, 1, v0
	v_cmp_ge_u32_e32 vcc, v5, v3
	s_nop 1
	v_cndmask_b32_e32 v0, v0, v6, vcc
	v_mul_lo_u32 v5, v3, v0
	v_add_u32_e32 v3, v5, v3
	v_cmp_ne_u32_e32 vcc, v4, v3
	s_and_saveexec_b64 s[0:1], vcc
	s_xor_b64 s[6:7], exec, s[0:1]
	s_cbranch_execz .LBB0_1512
	v_readlane_b32 s0, v252, 19
	v_readlane_b32 s1, v252, 20
	s_waitcnt lgkmcnt(0)
	v_add_u32_e32 v5, 1, v0
	v_mul_lo_u32 v5, v5, v2
	s_nop 3
	global_load_dword v2, v1, s[0:1] sc1
	s_waitcnt vmcnt(0)
	v_cmp_lt_u32_e32 vcc, v2, v5
	s_and_saveexec_b64 s[8:9], vcc
	s_cbranch_execz .LBB0_1511
	s_mov_b32 s0, 1
	s_mov_b64 s[10:11], 0
	s_branch .LBB0_1502

.LBB0_1504:
	v_readlane_b32 s26, v252, 19
	v_readlane_b32 s27, v252, 20
	s_add_i32 s0, s0, 1
	s_mov_b64 s[34:35], -1
	s_nop 2
	global_load_dword v2, v1, s[26:27] sc1
	s_waitcnt vmcnt(0)
	v_cmp_ge_u32_e32 vcc, v2, v5
	s_orn2_b64 s[30:31], vcc, exec
	s_branch .LBB0_1501

.LBB0_1515:
	s_or_b64 exec, exec, s[8:9]
	s_waitcnt vmcnt(0)
	v_readfirstlane_b32 s0, v3
	v_sub_u32_e32 v4, 0, v2
	s_mov_b64 s[8:9], -1
	v_add_u32_e32 v3, s0, v0
	v_cvt_f32_u32_e32 v0, v2
	v_readlane_b32 s0, v252, 21
	v_readlane_b32 s1, v252, 22
	v_rcp_iflag_f32_e32 v0, v0
	s_nop 0
	v_mul_f32_e32 v0, 0x4f7ffffe, v0
	v_cvt_u32_f32_e32 v0, v0
	v_mul_lo_u32 v4, v4, v0
	v_mul_hi_u32 v4, v0, v4
	v_add_u32_e32 v0, v0, v4
	v_mul_hi_u32 v0, v3, v0
	v_mul_lo_u32 v4, v0, v2
	v_sub_u32_e32 v4, v3, v4
	v_cmp_ge_u32_e32 vcc, v4, v2
	v_add_u32_e32 v5, 1, v0
	v_add_u32_e32 v3, 1, v3
	v_cndmask_b32_e32 v0, v0, v5, vcc
	v_sub_u32_e32 v5, v4, v2
	v_cndmask_b32_e32 v4, v4, v5, vcc
	v_cmp_ge_u32_e32 vcc, v4, v2
	v_add_u32_e32 v4, 1, v0
	s_nop 0
	v_cndmask_b32_e32 v0, v0, v4, vcc
	v_mul_lo_u32 v4, v2, v0
	v_add_u32_e32 v2, v4, v2
	v_mov_b32_e32 v5, v2
	v_cmp_ne_u32_e32 vcc, v3, v2
	v_mov_b64_e32 v[2:3], s[0:1]
	s_and_saveexec_b64 s[6:7], vcc
	s_cbranch_execz .LBB0_1527
	v_readlane_b32 s0, v252, 19
	v_readlane_b32 s1, v252, 20
	s_mov_b64 s[10:11], 0
	s_nop 3
	global_load_dword v2, v1, s[0:1] sc1
	s_waitcnt vmcnt(0)
	v_cmp_lt_u32_e32 vcc, v2, v5
	s_and_saveexec_b64 s[8:9], vcc
	s_cbranch_execz .LBB0_1526
	s_mov_b32 s0, 1
	s_branch .LBB0_1519

.LBB0_1590:
	v_readlane_b32 s4, v252, 15
	v_readlane_b32 s5, v252, 16
	v_cvt_f32_u32_e32 v0, v3
	v_sub_u32_e32 v5, 0, v3
	v_rcp_iflag_f32_e32 v0, v0
	s_nop 1
	global_atomic_add v4, v1, v236, s[4:5] sc0
	v_mul_f32_e32 v0, 0x4f7ffffe, v0
	v_cvt_u32_f32_e32 v0, v0
	v_mul_lo_u32 v5, v5, v0
	v_mul_hi_u32 v5, v0, v5
	v_add_u32_e32 v0, v0, v5
	s_waitcnt vmcnt(0)
	v_mul_hi_u32 v0, v4, v0
	v_mul_lo_u32 v5, v0, v3
	v_sub_u32_e32 v5, v4, v5
	v_add_u32_e32 v6, 1, v0
	v_cmp_ge_u32_e32 vcc, v5, v3
	v_add_u32_e32 v4, 1, v4
	s_nop 0
	v_cndmask_b32_e32 v0, v0, v6, vcc
	v_sub_u32_e32 v6, v5, v3
	v_cndmask_b32_e32 v5, v5, v6, vcc
	v_add_u32_e32 v6, 1, v0
	v_cmp_ge_u32_e32 vcc, v5, v3
	s_nop 1
	v_cndmask_b32_e32 v0, v0, v6, vcc
	v_mul_lo_u32 v5, v3, v0
	v_add_u32_e32 v3, v5, v3
	v_cmp_ne_u32_e32 vcc, v4, v3
	s_and_saveexec_b64 s[4:5], vcc
	s_xor_b64 s[4:5], exec, s[4:5]
	s_cbranch_execz .LBB0_1604
	v_readlane_b32 s6, v252, 19
	v_readlane_b32 s7, v252, 20
	s_waitcnt lgkmcnt(0)
	v_add_u32_e32 v5, 1, v0
	v_mul_lo_u32 v5, v5, v2
	s_nop 3
	global_load_dword v2, v1, s[6:7] sc1
	s_waitcnt vmcnt(0)
	v_cmp_lt_u32_e32 vcc, v2, v5
	s_and_saveexec_b64 s[6:7], vcc
	s_cbranch_execz .LBB0_1603
	s_mov_b32 s26, 1
	s_mov_b64 s[8:9], 0
	s_branch .LBB0_1594

.LBB0_1596:
	v_readlane_b32 s12, v252, 19
	v_readlane_b32 s13, v252, 20
	s_add_i32 s26, s26, 1
	s_mov_b64 s[28:29], -1
	s_nop 2
	global_load_dword v2, v1, s[12:13] sc1
	s_waitcnt vmcnt(0)
	v_cmp_ge_u32_e32 vcc, v2, v5
	s_orn2_b64 s[12:13], vcc, exec
	s_branch .LBB0_1593

.LBB0_1607:
	s_or_b64 exec, exec, s[6:7]
	s_waitcnt vmcnt(0)
	v_readfirstlane_b32 s4, v3
	v_sub_u32_e32 v4, 0, v2
	s_mov_b64 s[6:7], -1
	v_add_u32_e32 v3, s4, v0
	v_cvt_f32_u32_e32 v0, v2
	v_readlane_b32 s4, v252, 21
	v_readlane_b32 s5, v252, 22
	v_rcp_iflag_f32_e32 v0, v0
	s_nop 0
	v_mul_f32_e32 v0, 0x4f7ffffe, v0
	v_cvt_u32_f32_e32 v0, v0
	v_mul_lo_u32 v4, v4, v0
	v_mul_hi_u32 v4, v0, v4
	v_add_u32_e32 v0, v0, v4
	v_mul_hi_u32 v0, v3, v0
	v_mul_lo_u32 v4, v0, v2
	v_sub_u32_e32 v4, v3, v4
	v_cmp_ge_u32_e32 vcc, v4, v2
	v_add_u32_e32 v5, 1, v0
	v_add_u32_e32 v3, 1, v3
	v_cndmask_b32_e32 v0, v0, v5, vcc
	v_sub_u32_e32 v5, v4, v2
	v_cndmask_b32_e32 v4, v4, v5, vcc
	v_cmp_ge_u32_e32 vcc, v4, v2
	v_add_u32_e32 v4, 1, v0
	s_nop 0
	v_cndmask_b32_e32 v0, v0, v4, vcc
	v_mul_lo_u32 v4, v2, v0
	v_add_u32_e32 v2, v4, v2
	v_mov_b32_e32 v5, v2
	v_cmp_ne_u32_e32 vcc, v3, v2
	v_mov_b64_e32 v[2:3], s[4:5]
	s_and_saveexec_b64 s[4:5], vcc
	s_cbranch_execz .LBB0_1619
	v_readlane_b32 s6, v252, 19
	v_readlane_b32 s7, v252, 20
	s_mov_b64 s[8:9], 0
	s_nop 3
	global_load_dword v2, v1, s[6:7] sc1
	s_waitcnt vmcnt(0)
	v_cmp_lt_u32_e32 vcc, v2, v5
	s_and_saveexec_b64 s[6:7], vcc
	s_cbranch_execz .LBB0_1618
	s_mov_b32 s26, 1
	s_branch .LBB0_1611

.LBB0_1694:
	v_readlane_b32 s6, v252, 15
	v_readlane_b32 s7, v252, 16
	v_cvt_f32_u32_e32 v0, v3
	v_sub_u32_e32 v5, 0, v3
	v_rcp_iflag_f32_e32 v0, v0
	s_nop 1
	global_atomic_add v4, v1, v236, s[6:7] sc0
	v_mul_f32_e32 v0, 0x4f7ffffe, v0
	v_cvt_u32_f32_e32 v0, v0
	v_mul_lo_u32 v5, v5, v0
	v_mul_hi_u32 v5, v0, v5
	v_add_u32_e32 v0, v0, v5
	s_waitcnt vmcnt(0)
	v_mul_hi_u32 v0, v4, v0
	v_mul_lo_u32 v5, v0, v3
	v_sub_u32_e32 v5, v4, v5
	v_add_u32_e32 v6, 1, v0
	v_cmp_ge_u32_e32 vcc, v5, v3
	v_add_u32_e32 v4, 1, v4
	s_nop 0
	v_cndmask_b32_e32 v0, v0, v6, vcc
	v_sub_u32_e32 v6, v5, v3
	v_cndmask_b32_e32 v5, v5, v6, vcc
	v_add_u32_e32 v6, 1, v0
	v_cmp_ge_u32_e32 vcc, v5, v3
	s_nop 1
	v_cndmask_b32_e32 v0, v0, v6, vcc
	v_mul_lo_u32 v5, v3, v0
	v_add_u32_e32 v3, v5, v3
	v_cmp_ne_u32_e32 vcc, v4, v3
	s_and_saveexec_b64 s[6:7], vcc
	s_xor_b64 s[6:7], exec, s[6:7]
	s_cbranch_execz .LBB0_1708
	v_readlane_b32 s8, v252, 19
	v_readlane_b32 s9, v252, 20
	s_waitcnt lgkmcnt(0)
	v_add_u32_e32 v5, 1, v0
	v_mul_lo_u32 v5, v5, v2
	s_nop 3
	global_load_dword v2, v1, s[8:9] sc1
	s_waitcnt vmcnt(0)
	v_cmp_lt_u32_e32 vcc, v2, v5
	s_and_saveexec_b64 s[8:9], vcc
	s_cbranch_execz .LBB0_1707
	s_mov_b32 s26, 1
	s_mov_b64 s[10:11], 0
	s_branch .LBB0_1698

.LBB0_1700:
	v_readlane_b32 s28, v252, 19
	v_readlane_b32 s29, v252, 20
	s_add_i32 s26, s26, 1
	s_mov_b64 s[30:31], -1
	s_nop 2
	global_load_dword v2, v1, s[28:29] sc1
	s_waitcnt vmcnt(0)
	v_cmp_ge_u32_e32 vcc, v2, v5
	s_orn2_b64 s[28:29], vcc, exec
	s_branch .LBB0_1697

.LBB0_1711:
	s_or_b64 exec, exec, s[8:9]
	s_waitcnt vmcnt(0)
	v_readfirstlane_b32 s6, v3
	v_sub_u32_e32 v4, 0, v2
	s_mov_b64 s[8:9], -1
	v_add_u32_e32 v3, s6, v0
	v_cvt_f32_u32_e32 v0, v2
	v_readlane_b32 s6, v252, 21
	v_readlane_b32 s7, v252, 22
	v_rcp_iflag_f32_e32 v0, v0
	s_nop 0
	v_mul_f32_e32 v0, 0x4f7ffffe, v0
	v_cvt_u32_f32_e32 v0, v0
	v_mul_lo_u32 v4, v4, v0
	v_mul_hi_u32 v4, v0, v4
	v_add_u32_e32 v0, v0, v4
	v_mul_hi_u32 v0, v3, v0
	v_mul_lo_u32 v4, v0, v2
	v_sub_u32_e32 v4, v3, v4
	v_cmp_ge_u32_e32 vcc, v4, v2
	v_add_u32_e32 v5, 1, v0
	v_add_u32_e32 v3, 1, v3
	v_cndmask_b32_e32 v0, v0, v5, vcc
	v_sub_u32_e32 v5, v4, v2
	v_cndmask_b32_e32 v4, v4, v5, vcc
	v_cmp_ge_u32_e32 vcc, v4, v2
	v_add_u32_e32 v4, 1, v0
	s_nop 0
	v_cndmask_b32_e32 v0, v0, v4, vcc
	v_mul_lo_u32 v4, v2, v0
	v_add_u32_e32 v2, v4, v2
	v_mov_b32_e32 v5, v2
	v_cmp_ne_u32_e32 vcc, v3, v2
	v_mov_b64_e32 v[2:3], s[6:7]
	s_and_saveexec_b64 s[6:7], vcc
	s_cbranch_execz .LBB0_1723
	v_readlane_b32 s8, v252, 19
	v_readlane_b32 s9, v252, 20
	s_mov_b64 s[10:11], 0
	s_nop 3
	global_load_dword v2, v1, s[8:9] sc1
	s_waitcnt vmcnt(0)
	v_cmp_lt_u32_e32 vcc, v2, v5
	s_and_saveexec_b64 s[8:9], vcc
	s_cbranch_execz .LBB0_1722
	s_mov_b32 s26, 1
	s_branch .LBB0_1715

.LBB0_2186:
	v_readlane_b32 s4, v252, 15
	v_readlane_b32 s5, v252, 16
	v_cvt_f32_u32_e32 v0, v3
	v_sub_u32_e32 v5, 0, v3
	v_rcp_iflag_f32_e32 v0, v0
	s_nop 1
	global_atomic_add v4, v1, v236, s[4:5] sc0
	v_mul_f32_e32 v0, 0x4f7ffffe, v0
	v_cvt_u32_f32_e32 v0, v0
	v_mul_lo_u32 v5, v5, v0
	v_mul_hi_u32 v5, v0, v5
	v_add_u32_e32 v0, v0, v5
	s_waitcnt vmcnt(0)
	v_mul_hi_u32 v0, v4, v0
	v_mul_lo_u32 v5, v0, v3
	v_sub_u32_e32 v5, v4, v5
	v_add_u32_e32 v6, 1, v0
	v_cmp_ge_u32_e32 vcc, v5, v3
	v_add_u32_e32 v4, 1, v4
	s_nop 0
	v_cndmask_b32_e32 v0, v0, v6, vcc
	v_sub_u32_e32 v6, v5, v3
	v_cndmask_b32_e32 v5, v5, v6, vcc
	v_add_u32_e32 v6, 1, v0
	v_cmp_ge_u32_e32 vcc, v5, v3
	s_nop 1
	v_cndmask_b32_e32 v0, v0, v6, vcc
	v_mul_lo_u32 v5, v3, v0
	v_add_u32_e32 v3, v5, v3
	v_cmp_ne_u32_e32 vcc, v4, v3
	s_and_saveexec_b64 s[4:5], vcc
	s_xor_b64 s[4:5], exec, s[4:5]
	s_cbranch_execz .LBB0_2200
	v_readlane_b32 s6, v252, 19
	v_readlane_b32 s7, v252, 20
	s_waitcnt lgkmcnt(0)
	v_add_u32_e32 v5, 1, v0
	v_mul_lo_u32 v5, v5, v2
	s_nop 3
	global_load_dword v2, v1, s[6:7] sc1
	s_waitcnt vmcnt(0)
	v_cmp_lt_u32_e32 vcc, v2, v5
	s_and_saveexec_b64 s[6:7], vcc
	s_cbranch_execz .LBB0_2199
	s_mov_b32 s23, 1
	s_mov_b64 s[8:9], 0
	s_branch .LBB0_2190

.LBB0_2192:
	v_readlane_b32 s12, v252, 19
	v_readlane_b32 s13, v252, 20
	s_add_i32 s23, s23, 1
	s_mov_b64 s[28:29], -1
	s_nop 2
	global_load_dword v2, v1, s[12:13] sc1
	s_waitcnt vmcnt(0)
	v_cmp_ge_u32_e32 vcc, v2, v5
	s_orn2_b64 s[12:13], vcc, exec
	s_branch .LBB0_2189

.LBB0_2203:
	s_or_b64 exec, exec, s[6:7]
	s_waitcnt vmcnt(0)
	v_readfirstlane_b32 s4, v3
	v_sub_u32_e32 v4, 0, v2
	s_mov_b64 s[6:7], -1
	v_add_u32_e32 v3, s4, v0
	v_cvt_f32_u32_e32 v0, v2
	v_readlane_b32 s4, v252, 21
	v_readlane_b32 s5, v252, 22
	v_rcp_iflag_f32_e32 v0, v0
	s_nop 0
	v_mul_f32_e32 v0, 0x4f7ffffe, v0
	v_cvt_u32_f32_e32 v0, v0
	v_mul_lo_u32 v4, v4, v0
	v_mul_hi_u32 v4, v0, v4
	v_add_u32_e32 v0, v0, v4
	v_mul_hi_u32 v0, v3, v0
	v_mul_lo_u32 v4, v0, v2
	v_sub_u32_e32 v4, v3, v4
	v_cmp_ge_u32_e32 vcc, v4, v2
	v_add_u32_e32 v5, 1, v0
	v_add_u32_e32 v3, 1, v3
	v_cndmask_b32_e32 v0, v0, v5, vcc
	v_sub_u32_e32 v5, v4, v2
	v_cndmask_b32_e32 v4, v4, v5, vcc
	v_cmp_ge_u32_e32 vcc, v4, v2
	v_add_u32_e32 v4, 1, v0
	s_nop 0
	v_cndmask_b32_e32 v0, v0, v4, vcc
	v_mul_lo_u32 v4, v2, v0
	v_add_u32_e32 v2, v4, v2
	v_mov_b32_e32 v5, v2
	v_cmp_ne_u32_e32 vcc, v3, v2
	v_mov_b64_e32 v[2:3], s[4:5]
	s_and_saveexec_b64 s[4:5], vcc
	s_cbranch_execz .LBB0_2215
	v_readlane_b32 s6, v252, 19
	v_readlane_b32 s7, v252, 20
	s_mov_b64 s[8:9], 0
	s_nop 3
	global_load_dword v2, v1, s[6:7] sc1
	s_waitcnt vmcnt(0)
	v_cmp_lt_u32_e32 vcc, v2, v5
	s_and_saveexec_b64 s[6:7], vcc
	s_cbranch_execz .LBB0_2214
	s_mov_b32 s23, 1
	s_branch .LBB0_2207
